# prologue S5 discretisation: runs on workgroups 248-255 instead of 0-7, B-bar inputs loaded with 8 wide loads in flight
# baseline (speedup 1.0000x reference)
;     ...
;     for (int i = bid * NTHR + tid; i < 4096; i += nb * NTHR) {
;         const int dg = i >> 6, p = i & 63;
;         const float are = P.in[26][i], aim = P.in[27][i];
;         const float dt = expf(P.in[28][dg]);
;         const float mag = expf(are * dt);
;         const float abr = mag * cosf(aim * dt), abi = mag * sinf(aim * dt);
;         ((float2*)(P.ws + WS_ABAR))[i] = make_float2(abr, abi);
.LBB0_280:
	s_xor_b32 s0, s44, 0xff
	v_lshl_or_b32 v2, s0, 9, v0
	s_movk_i32 s0, 0x1000
	v_cmp_gt_i32_e32 vcc, s0, v2
	s_and_saveexec_b64 s[2:3], vcc
	s_cbranch_execz .LBB0_295
	v_readlane_b32 s16, v252, 19
	s_lshl_b32 s4, s4, 9
	v_readlane_b32 s18, v252, 21
	v_readlane_b32 s19, v252, 22
	s_add_u32 s10, s18, 0x4f28000
	s_addc_u32 s11, s19, 0
	s_add_u32 s12, s18, 0x4f30000
	s_addc_u32 s13, s19, 0
	v_ashrrev_i32_e32 v3, 31, v2
	s_add_u32 s14, s18, 0x4fb8000
	v_lshlrev_b64 v[6:7], 7, v[2:3]
	v_lshlrev_b32_e32 v4, 1, v202
	v_readlane_b32 s17, v252, 20
	s_addc_u32 s15, s19, 0
	v_lshl_add_u64 v[6:7], s[18:19], 0, v[6:7]
	s_mov_b64 s[0:1], 0x4f38018
	s_ashr_i32 s5, s4, 31
	v_lshlrev_b64 v[10:11], 6, v[2:3]
	v_mov_b32_e32 v1, v4
	v_lshl_add_u64 v[6:7], v[6:7], 0, s[0:1]
	s_lshl_b64 s[16:17], s[4:5], 7
	v_lshl_add_u64 v[8:9], s[64:65], 0, v[10:11]
	s_lshl_b64 s[18:19], s[4:5], 6
	v_lshl_add_u64 v[10:11], s[62:63], 0, v[10:11]
	s_mov_b64 s[20:21], 0
	s_mov_b32 s5, 0x3fb8aa3b
	s_mov_b32 s28, 0xc2ce8ed0
	s_mov_b32 s23, 0
	s_mov_b32 s29, 0x42b17218
	v_mov_b32_e32 v5, 0x7f800000
	s_mov_b32 s30, 0xfe5163ab
	v_mov_b32_e32 v13, 0
	s_mov_b32 s31, 0x3c439041
	s_mov_b32 s34, 0xdb629599
	s_mov_b32 s35, 0xf534ddc0
	s_mov_b32 s36, 0xfc2757d1
	s_mov_b32 s37, 0x4e441529
	s_mov_b32 s38, 0xa2f9836e
	s_mov_b32 s39, 0x3fc90fda
	s_mov_b32 s40, 0xbfc90fda
	v_mov_b32_e32 v24, 0x3c0881c4
	v_mov_b32_e32 v25, 0xbab64f3b
	v_mov_b32_e32 v15, 2.0
	v_not_b32_e32 v26, 63
	v_not_b32_e32 v27, 31
	v_mov_b32_e32 v28, 0x7fc00000

;     ...
;         const float nr = abr - 1.f, ni = abi, den = are * are + aim * aim;
;         const float cr = (nr * are + ni * aim) / den, ci = (ni * are - nr * aim) / den;
;         float2* bb = (float2*)(P.ws + WS_BBAR) + (size_t)i * 16;
; #pragma unroll 4
;         for (int k = 0; k < 16; ++k) {
;             const float br = P.in[29][(size_t)i * 16 + k], bi = P.in[30][(size_t)i * 16 + k];
;             bb[k] = make_float2(cr * br - ci * bi, cr * bi + ci * br);
;         }
;         bfr* cm = (bfr*)(P.ws + WS_CMAT) + (size_t)dg * 16 * 128;
; #pragma unroll 4
;         for (int n = 0; n < 16; ++n) {
;             const float c_re = P.in[31][((size_t)dg * 16 + n) * 64 + p], c_im = P.in[32][((size_t)dg * 16 + n) * 64 + p];
.LBB0_291:
	global_load_dwordx4 v[60:63], v[8:9], off
	global_load_dwordx4 v[64:67], v[8:9], off offset:16
	global_load_dwordx4 v[68:71], v[8:9], off offset:32
	global_load_dwordx4 v[72:75], v[8:9], off offset:48
	global_load_dwordx4 v[76:79], v[10:11], off
	global_load_dwordx4 v[80:83], v[10:11], off offset:16
	global_load_dwordx4 v[84:87], v[10:11], off offset:32
	global_load_dwordx4 v[88:91], v[10:11], off offset:48
	s_waitcnt vmcnt(0)
	v_mul_f32_e32 v92, v20, v60
	v_mul_f32_e32 v93, v21, v60
	v_fma_f32 v96, v18, v76, -v92
	v_fma_f32 v97, v19, v76, v93
	v_mul_f32_e32 v92, v20, v61
	v_mul_f32_e32 v93, v21, v61
	v_fma_f32 v98, v18, v77, -v92
	v_fma_f32 v99, v19, v77, v93
	v_mul_f32_e32 v92, v20, v62
	v_mul_f32_e32 v93, v21, v62
	v_fma_f32 v100, v18, v78, -v92
	v_fma_f32 v101, v19, v78, v93
	v_mul_f32_e32 v92, v20, v63
	v_mul_f32_e32 v93, v21, v63
	v_fma_f32 v102, v18, v79, -v92
	v_fma_f32 v103, v19, v79, v93
	v_mul_f32_e32 v92, v20, v64
	v_mul_f32_e32 v93, v21, v64
	v_fma_f32 v104, v18, v80, -v92
	v_fma_f32 v105, v19, v80, v93
	v_mul_f32_e32 v92, v20, v65
	v_mul_f32_e32 v93, v21, v65
	v_fma_f32 v106, v18, v81, -v92
	v_fma_f32 v107, v19, v81, v93
	v_mul_f32_e32 v92, v20, v66
	v_mul_f32_e32 v93, v21, v66
	v_fma_f32 v108, v18, v82, -v92
	v_fma_f32 v109, v19, v82, v93
	v_mul_f32_e32 v92, v20, v67
	v_mul_f32_e32 v93, v21, v67
	v_fma_f32 v110, v18, v83, -v92
	v_fma_f32 v111, v19, v83, v93
	v_mul_f32_e32 v92, v20, v68
	v_mul_f32_e32 v93, v21, v68
	v_fma_f32 v112, v18, v84, -v92
	v_fma_f32 v113, v19, v84, v93
	v_mul_f32_e32 v92, v20, v69
	v_mul_f32_e32 v93, v21, v69
	v_fma_f32 v114, v18, v85, -v92
	v_fma_f32 v115, v19, v85, v93
	v_mul_f32_e32 v92, v20, v70
	v_mul_f32_e32 v93, v21, v70
	v_fma_f32 v116, v18, v86, -v92
	v_fma_f32 v117, v19, v86, v93
	v_mul_f32_e32 v92, v20, v71
	v_mul_f32_e32 v93, v21, v71
	v_fma_f32 v118, v18, v87, -v92
	v_fma_f32 v119, v19, v87, v93
	v_mul_f32_e32 v92, v20, v72
	v_mul_f32_e32 v93, v21, v72
	v_fma_f32 v120, v18, v88, -v92
	v_fma_f32 v121, v19, v88, v93
	v_mul_f32_e32 v92, v20, v73
	v_mul_f32_e32 v93, v21, v73
	v_fma_f32 v122, v18, v89, -v92
	v_fma_f32 v123, v19, v89, v93
	v_mul_f32_e32 v92, v20, v74
	v_mul_f32_e32 v93, v21, v74
	v_fma_f32 v124, v18, v90, -v92
	v_fma_f32 v125, v19, v90, v93
	v_mul_f32_e32 v92, v20, v75
	v_mul_f32_e32 v93, v21, v75
	v_fma_f32 v126, v18, v91, -v92
	v_fma_f32 v127, v19, v91, v93
	global_store_dwordx4 v[22:23], v[96:99], off offset:-24
	global_store_dwordx4 v[22:23], v[100:103], off offset:-8
	global_store_dwordx4 v[22:23], v[104:107], off offset:8
	global_store_dwordx4 v[22:23], v[108:111], off offset:24
	global_store_dwordx4 v[22:23], v[112:115], off offset:40
	global_store_dwordx4 v[22:23], v[116:119], off offset:56
	global_store_dwordx4 v[22:23], v[120:123], off offset:72
	global_store_dwordx4 v[22:23], v[124:127], off offset:88
	v_lshlrev_b64 v[18:19], 12, v[16:17]
	v_lshlrev_b64 v[16:17], 10, v[16:17]
	v_readlane_b32 s76, v252, 3
	v_or_b32_e32 v16, v16, v202
	v_readlane_b32 s77, v252, 4
	v_lshl_add_u64 v[18:19], s[14:15], 0, v[18:19]
	v_mov_b32_e32 v20, v16
	v_mov_b32_e32 v21, v17
	s_mov_b32 s6, 1
	s_mov_b32 s7, 0
	s_mov_b32 s8, 16
	v_readlane_b32 s78, v252, 5
	v_readlane_b32 s79, v252, 6
	s_mov_b64 s[68:69], s[76:77]
	v_readlane_b32 s80, v252, 7
	v_readlane_b32 s81, v252, 8
	v_readlane_b32 s82, v252, 9
	v_readlane_b32 s83, v252, 10
	v_readlane_b32 s84, v252, 11
	v_readlane_b32 s85, v252, 12
	v_readlane_b32 s86, v252, 13
	v_readlane_b32 s87, v252, 14
	v_readlane_b32 s88, v252, 15
	v_readlane_b32 s89, v252, 16
	v_readlane_b32 s90, v252, 17
	v_readlane_b32 s91, v252, 18
	s_mov_b64 s[70:71], s[78:79]
